# agg2: stage-0 row gathers issued before softmax + 4-row ring re-issue in stage loop (no gain: agg2 is throughput-bound)
# baseline (speedup 1.0000x reference)
.LBB2_21:
	s_endpgm
	s_endpgm

.LBB3_37:
	s_endpgm
	s_nop 0
	s_nop 0
	s_nop 0
	s_nop 0
	s_nop 0
	s_nop 0
	s_nop 0
	s_nop 0
	s_nop 0
	s_nop 0
	s_endpgm

.LBB4_3:
	s_waitcnt vmcnt(4)
	v_lshlrev_b32_sdwa v8, v59, v60 dst_sel:DWORD dst_unused:UNUSED_PAD src0_sel:DWORD src1_sel:WORD_0
	s_waitcnt vmcnt(3)
	v_lshlrev_b32_sdwa v9, v59, v62 dst_sel:DWORD dst_unused:UNUSED_PAD src0_sel:DWORD src1_sel:WORD_0
	s_waitcnt vmcnt(2)
	v_lshlrev_b32_sdwa v10, v59, v61 dst_sel:DWORD dst_unused:UNUSED_PAD src0_sel:DWORD src1_sel:WORD_0
	s_waitcnt vmcnt(1)
	v_lshlrev_b32_sdwa v11, v59, v63 dst_sel:DWORD dst_unused:UNUSED_PAD src0_sel:DWORD src1_sel:WORD_0
	global_load_ushort v40, v8, s[10:11]
	global_load_ushort v41, v9, s[10:11]
	global_load_ushort v42, v10, s[10:11]
	global_load_ushort v43, v11, s[10:11]
	v_mov_b64_e32 v[36:37], v[70:71]
	v_mov_b32_e32 v8, v53
	v_add_u32_e32 v9, s20, v31
	v_mul_u32_u24_sdwa v10, v60, s21 dst_sel:DWORD dst_unused:UNUSED_PAD src0_sel:WORD_0 src1_sel:DWORD
	v_mul_u32_u24_sdwa v11, v62, s21 dst_sel:DWORD dst_unused:UNUSED_PAD src0_sel:WORD_0 src1_sel:DWORD
	v_mul_u32_u24_sdwa v14, v61, s21 dst_sel:DWORD dst_unused:UNUSED_PAD src0_sel:WORD_0 src1_sel:DWORD
	v_mul_u32_u24_sdwa v15, v63, s21 dst_sel:DWORD dst_unused:UNUSED_PAD src0_sel:WORD_0 src1_sel:DWORD
	v_min_i32_e32 v53, 0x30d3, v9
	ds_write2_b32 v56, v10, v11 offset1:16
	ds_write2_b32 v56, v14, v15 offset0:32 offset1:48
	v_add_u32_e32 v9, -1, v37
	v_add_u32_e32 v11, v36, v49
	v_add_u32_e32 v14, v50, v36
	v_add_u32_e32 v15, v51, v36
	v_add_u32_e32 v16, v52, v36
	v_lshl_or_b32 v8, v8, 2, v48
	v_lshl_or_b32 v10, v53, 2, v48
	v_min_i32_e32 v17, v11, v9
	v_min_i32_e32 v14, v14, v9
	v_min_i32_e32 v15, v15, v9
	v_min_i32_e32 v16, v16, v9
	v_ashrrev_i32_e32 v9, 31, v8
	v_ashrrev_i32_e32 v11, 31, v10
	v_max_i32_e32 v17, 0, v17
	v_max_i32_e32 v14, 0, v14
	v_max_i32_e32 v15, 0, v15
	v_max_i32_e32 v16, 0, v16
	v_lshl_add_u64 v[8:9], v[8:9], 1, s[12:13]
	s_waitcnt vmcnt(4)
	v_cvt_f32_f16_e32 v65, v64
	v_lshl_add_u64 v[10:11], v[10:11], 2, s[4:5]
	v_lshlrev_b32_e32 v17, 1, v17
	v_lshlrev_b32_e32 v14, 1, v14
	v_lshlrev_b32_e32 v15, 1, v15
	v_lshlrev_b32_e32 v16, 1, v16
	global_load_ushort v64, v[8:9], off
	global_load_dwordx2 v[70:71], v[10:11], off
	global_load_ushort v60, v17, s[6:7]
	global_load_ushort v62, v14, s[6:7]
	global_load_ushort v61, v15, s[6:7]
	global_load_ushort v63, v16, s[6:7]
	ds_read_b128 v[72:75], v55
	s_waitcnt lgkmcnt(0)
	v_add_u32_e32 v72, v72, v30
	v_add_u32_e32 v73, v73, v30
	v_add_u32_e32 v74, v74, v30
	v_add_u32_e32 v75, v75, v30
	global_load_dwordx4 v[8:11], v72, s[8:9]
	global_load_dwordx4 v[12:15], v73, s[8:9]
	global_load_dwordx4 v[16:19], v74, s[8:9]
	global_load_dwordx4 v[20:23], v75, s[8:9]
	v_sub_u32_e32 v67, v35, v34
	v_med3_i32 v44, v67, 0, 60
	v_cmp_gt_i32_e32 vcc, v67, v49
	v_readlane_b32 s2, v44, 0
	v_readlane_b32 s3, v44, 16
	v_readlane_b32 s16, v44, 32
	v_readlane_b32 s17, v44, 48
	s_max_i32 s16, s16, s17
	s_waitcnt vmcnt(13)
	v_cvt_f32_f16_e32 v45, v40
	s_waitcnt vmcnt(12)
	v_cvt_f32_f16_e32 v46, v41
	s_waitcnt vmcnt(11)
	v_cvt_f32_f16_e32 v47, v42
	s_waitcnt vmcnt(10)
	v_cvt_f32_f16_e32 v39, v43
	v_add_f32_e32 v45, v65, v45
	v_add_f32_e32 v46, v65, v46
	v_mul_f32_e32 v68, 0x3e4ccccd, v45
	v_add_f32_e32 v47, v65, v47
	v_mul_f32_e32 v69, 0x3e4ccccd, v46
	v_max_f32_e32 v45, v45, v68
	v_add_f32_e32 v39, v65, v39
	v_mul_f32_e32 v72, 0x3e4ccccd, v47
	v_max_f32_e32 v46, v46, v69
	v_cndmask_b32_e32 v45, v58, v45, vcc
	v_cmp_lt_u32_e32 vcc, v50, v44
	v_mul_f32_e32 v73, 0x3e4ccccd, v39
	v_max_f32_e32 v47, v47, v72
	v_cndmask_b32_e32 v46, v58, v46, vcc
	v_cmp_lt_u32_e32 vcc, v51, v44
	v_max_f32_e32 v39, v39, v73
	s_nop 0
	v_cndmask_b32_e32 v47, v58, v47, vcc
	v_cmp_lt_u32_e32 vcc, v52, v44
	s_nop 1
	v_cndmask_b32_e32 v44, v58, v39, vcc
	v_max3_f32 v39, v45, s22, v46
	v_max3_f32 v39, v39, v47, v44
	s_nop 1
	v_mov_b32_dpp v68, v39 quad_perm:[1,0,3,2] row_mask:0xf bank_mask:0xf bound_ctrl:1
	v_max_f32_e32 v68, v68, v68
	v_max_f32_e32 v39, v39, v68
	s_nop 1
	v_mov_b32_dpp v68, v39 quad_perm:[2,3,0,1] row_mask:0xf bank_mask:0xf bound_ctrl:1
	v_max_f32_e32 v68, v68, v68
	v_max_f32_e32 v39, v39, v68
	s_nop 1
	v_mov_b32_dpp v68, v39 row_half_mirror row_mask:0xf bank_mask:0xf bound_ctrl:1
	v_max_f32_e32 v68, v68, v68
	v_max_f32_e32 v39, v39, v68
	s_nop 1
	v_mov_b32_dpp v68, v39 row_mirror row_mask:0xf bank_mask:0xf bound_ctrl:1
	v_max3_f32 v39, v39, v68, s22
	v_cmp_neq_f32_e32 vcc, s22, v39
	v_mov_b32_e32 v68, s3
	s_nop 0
	v_cndmask_b32_e32 v66, 0, v39, vcc
	v_sub_f32_e32 v45, v45, v66
	v_sub_f32_e32 v46, v46, v66
	v_sub_f32_e32 v47, v47, v66
	v_sub_f32_e32 v44, v44, v66
	v_exp_f32_e32 v45, v45
	v_exp_f32_e32 v46, v46
	v_exp_f32_e32 v47, v47
	v_exp_f32_e32 v44, v44
	v_sub_f32_e32 v39, 0xff800000, v66
	v_exp_f32_e32 v39, v39
	ds_write2_b32 v57, v45, v46 offset1:16
	ds_write2_b32 v57, v47, v44 offset0:32 offset1:48
	v_mov_b32_e32 v44, s16
	v_max3_i32 v44, s2, v68, v44
	v_cmp_gt_i32_e32 vcc, 1, v44
	v_mul_f32_e32 v38, 0, v39
	v_readfirstlane_b32 s2, v44
	s_cbranch_vccnz .LBB4_9
	s_add_i32 s2, s2, 11
	s_mul_hi_i32 s2, s2, 0x2aaaaaab
	s_lshr_b32 s3, s2, 31
	s_ashr_i32 s2, s2, 1
	s_add_i32 s2, s2, s3
	s_max_i32 s3, s2, 1
	s_mov_b32 s16, 0
	v_mov_b32_e32 v47, v54
	v_mov_b32_e32 v46, v38
	v_mov_b32_e32 v45, v38
	v_mov_b32_e32 v44, v38
	v_mov_b32_e32 v40, v38
	v_mov_b32_e32 v41, v38
	v_mov_b32_e32 v42, v38
	v_mov_b32_e32 v43, v38
	v_mov_b32_e32 v39, v38
.Lagg2_ring:
	ds_read_b128 v[24:27], v47
	s_add_i32 s16, s16, 1
	s_cmp_ge_i32 s16, s2
	s_cbranch_scc1 .Lagg2_ring_last
	ds_read_b128 v[72:75], v47 offset:4400
	s_waitcnt lgkmcnt(0)
	v_add_u32_e32 v72, v72, v30
	v_add_u32_e32 v73, v73, v30
	v_add_u32_e32 v74, v74, v30
	v_add_u32_e32 v75, v75, v30
	s_waitcnt vmcnt(3)
	v_fma_mix_f32 v44, v8, v24, v44 op_sel_hi:[1,0,0]
	v_fma_mix_f32 v45, v8, v24, v45 op_sel:[1,0,0] op_sel_hi:[1,0,0]
	v_fma_mix_f32 v46, v9, v24, v46 op_sel_hi:[1,0,0]
	v_fma_mix_f32 v38, v9, v24, v38 op_sel:[1,0,0] op_sel_hi:[1,0,0]
	v_fma_mix_f32 v40, v10, v24, v40 op_sel_hi:[1,0,0]
	v_fma_mix_f32 v41, v10, v24, v41 op_sel:[1,0,0] op_sel_hi:[1,0,0]
	v_fma_mix_f32 v42, v11, v24, v42 op_sel_hi:[1,0,0]
	v_fma_mix_f32 v43, v11, v24, v43 op_sel:[1,0,0] op_sel_hi:[1,0,0]
	global_load_dwordx4 v[8:11], v72, s[8:9]
	s_waitcnt vmcnt(3)
	v_fma_mix_f32 v44, v12, v25, v44 op_sel_hi:[1,0,0]
	v_fma_mix_f32 v45, v12, v25, v45 op_sel:[1,0,0] op_sel_hi:[1,0,0]
	v_fma_mix_f32 v46, v13, v25, v46 op_sel_hi:[1,0,0]
	v_fma_mix_f32 v38, v13, v25, v38 op_sel:[1,0,0] op_sel_hi:[1,0,0]
	v_fma_mix_f32 v40, v14, v25, v40 op_sel_hi:[1,0,0]
	v_fma_mix_f32 v41, v14, v25, v41 op_sel:[1,0,0] op_sel_hi:[1,0,0]
	v_fma_mix_f32 v42, v15, v25, v42 op_sel_hi:[1,0,0]
	v_fma_mix_f32 v43, v15, v25, v43 op_sel:[1,0,0] op_sel_hi:[1,0,0]
	global_load_dwordx4 v[12:15], v73, s[8:9]
	s_waitcnt vmcnt(3)
	v_fma_mix_f32 v44, v16, v26, v44 op_sel_hi:[1,0,0]
	v_fma_mix_f32 v45, v16, v26, v45 op_sel:[1,0,0] op_sel_hi:[1,0,0]
	v_fma_mix_f32 v46, v17, v26, v46 op_sel_hi:[1,0,0]
	v_fma_mix_f32 v38, v17, v26, v38 op_sel:[1,0,0] op_sel_hi:[1,0,0]
	v_fma_mix_f32 v40, v18, v26, v40 op_sel_hi:[1,0,0]
	v_fma_mix_f32 v41, v18, v26, v41 op_sel:[1,0,0] op_sel_hi:[1,0,0]
	v_fma_mix_f32 v42, v19, v26, v42 op_sel_hi:[1,0,0]
	v_fma_mix_f32 v43, v19, v26, v43 op_sel:[1,0,0] op_sel_hi:[1,0,0]
	global_load_dwordx4 v[16:19], v74, s[8:9]
	s_waitcnt vmcnt(3)
	v_fma_mix_f32 v44, v20, v27, v44 op_sel_hi:[1,0,0]
	v_fma_mix_f32 v45, v20, v27, v45 op_sel:[1,0,0] op_sel_hi:[1,0,0]
	v_fma_mix_f32 v46, v21, v27, v46 op_sel_hi:[1,0,0]
	v_fma_mix_f32 v38, v21, v27, v38 op_sel:[1,0,0] op_sel_hi:[1,0,0]
	v_fma_mix_f32 v40, v22, v27, v40 op_sel_hi:[1,0,0]
	v_fma_mix_f32 v41, v22, v27, v41 op_sel:[1,0,0] op_sel_hi:[1,0,0]
	v_fma_mix_f32 v42, v23, v27, v42 op_sel_hi:[1,0,0]
	v_fma_mix_f32 v43, v23, v27, v43 op_sel:[1,0,0] op_sel_hi:[1,0,0]
	global_load_dwordx4 v[20:23], v75, s[8:9]
	v_add_f32_e32 v68, v24, v25
	v_add_f32_e32 v69, v26, v27
	v_add_u32_e32 v47, 48, v47
	v_add_f32_e32 v68, v68, v69
	v_add_f32_e32 v39, v39, v68
	s_branch .Lagg2_ring
.Lagg2_ring_last:
	s_waitcnt lgkmcnt(0)
	s_waitcnt vmcnt(3)
	v_fma_mix_f32 v44, v8, v24, v44 op_sel_hi:[1,0,0]
	v_fma_mix_f32 v45, v8, v24, v45 op_sel:[1,0,0] op_sel_hi:[1,0,0]
	v_fma_mix_f32 v46, v9, v24, v46 op_sel_hi:[1,0,0]
	v_fma_mix_f32 v38, v9, v24, v38 op_sel:[1,0,0] op_sel_hi:[1,0,0]
	v_fma_mix_f32 v40, v10, v24, v40 op_sel_hi:[1,0,0]
	v_fma_mix_f32 v41, v10, v24, v41 op_sel:[1,0,0] op_sel_hi:[1,0,0]
	v_fma_mix_f32 v42, v11, v24, v42 op_sel_hi:[1,0,0]
	v_fma_mix_f32 v43, v11, v24, v43 op_sel:[1,0,0] op_sel_hi:[1,0,0]
	s_waitcnt vmcnt(2)
	v_fma_mix_f32 v44, v12, v25, v44 op_sel_hi:[1,0,0]
	v_fma_mix_f32 v45, v12, v25, v45 op_sel:[1,0,0] op_sel_hi:[1,0,0]
	v_fma_mix_f32 v46, v13, v25, v46 op_sel_hi:[1,0,0]
	v_fma_mix_f32 v38, v13, v25, v38 op_sel:[1,0,0] op_sel_hi:[1,0,0]
	v_fma_mix_f32 v40, v14, v25, v40 op_sel_hi:[1,0,0]
	v_fma_mix_f32 v41, v14, v25, v41 op_sel:[1,0,0] op_sel_hi:[1,0,0]
	v_fma_mix_f32 v42, v15, v25, v42 op_sel_hi:[1,0,0]
	v_fma_mix_f32 v43, v15, v25, v43 op_sel:[1,0,0] op_sel_hi:[1,0,0]
	s_waitcnt vmcnt(1)
	v_fma_mix_f32 v44, v16, v26, v44 op_sel_hi:[1,0,0]
	v_fma_mix_f32 v45, v16, v26, v45 op_sel:[1,0,0] op_sel_hi:[1,0,0]
	v_fma_mix_f32 v46, v17, v26, v46 op_sel_hi:[1,0,0]
	v_fma_mix_f32 v38, v17, v26, v38 op_sel:[1,0,0] op_sel_hi:[1,0,0]
	v_fma_mix_f32 v40, v18, v26, v40 op_sel_hi:[1,0,0]
	v_fma_mix_f32 v41, v18, v26, v41 op_sel:[1,0,0] op_sel_hi:[1,0,0]
	v_fma_mix_f32 v42, v19, v26, v42 op_sel_hi:[1,0,0]
	v_fma_mix_f32 v43, v19, v26, v43 op_sel:[1,0,0] op_sel_hi:[1,0,0]
	s_waitcnt vmcnt(0)
	v_fma_mix_f32 v44, v20, v27, v44 op_sel_hi:[1,0,0]
	v_fma_mix_f32 v45, v20, v27, v45 op_sel:[1,0,0] op_sel_hi:[1,0,0]
	v_fma_mix_f32 v46, v21, v27, v46 op_sel_hi:[1,0,0]
	v_fma_mix_f32 v38, v21, v27, v38 op_sel:[1,0,0] op_sel_hi:[1,0,0]
	v_fma_mix_f32 v40, v22, v27, v40 op_sel_hi:[1,0,0]
	v_fma_mix_f32 v41, v22, v27, v41 op_sel:[1,0,0] op_sel_hi:[1,0,0]
	v_fma_mix_f32 v42, v23, v27, v42 op_sel_hi:[1,0,0]
	v_fma_mix_f32 v43, v23, v27, v43 op_sel:[1,0,0] op_sel_hi:[1,0,0]
	v_add_f32_e32 v68, v24, v25
	v_add_f32_e32 v69, v26, v27
	v_add_f32_e32 v68, v68, v69
	v_add_f32_e32 v39, v39, v68

.LBB4_9:
	s_waitcnt vmcnt(0)
	v_mov_b32_e32 v39, v38
	v_mov_b64_e32 v[42:43], v[38:39]
	v_mov_b64_e32 v[40:41], v[38:39]
	v_mov_b64_e32 v[46:47], v[38:39]
	v_mov_b64_e32 v[44:45], v[38:39]

	.amdhsa_kernel _Z5k_aggILi1ELi40ELi5ELi5ELb1EEvPKiPKtPKDF16_PKfS7_S7_PvS5_S7_S7_PDF16_PfSA_
		.amdhsa_group_segment_fixed_size 8704
		.amdhsa_private_segment_fixed_size 0
		.amdhsa_kernarg_size 360
		.amdhsa_user_sgpr_count 2
		.amdhsa_user_sgpr_dispatch_ptr 0
		.amdhsa_user_sgpr_queue_ptr 0
		.amdhsa_user_sgpr_kernarg_segment_ptr 1
		.amdhsa_user_sgpr_dispatch_id 0
		.amdhsa_user_sgpr_kernarg_preload_length 0
		.amdhsa_user_sgpr_kernarg_preload_offset 0
		.amdhsa_user_sgpr_private_segment_size 0
		.amdhsa_uses_dynamic_stack 0
		.amdhsa_enable_private_segment 0
		.amdhsa_system_sgpr_workgroup_id_x 1
		.amdhsa_system_sgpr_workgroup_id_y 0
		.amdhsa_system_sgpr_workgroup_id_z 0
		.amdhsa_system_sgpr_workgroup_info 0
		.amdhsa_system_vgpr_workitem_id 0
		.amdhsa_next_free_vgpr 76
		.amdhsa_next_free_sgpr 25
		.amdhsa_accum_offset 76
		.amdhsa_reserve_vcc 1
		.amdhsa_float_round_mode_32 0
		.amdhsa_float_round_mode_16_64 0
		.amdhsa_float_denorm_mode_32 3
		.amdhsa_float_denorm_mode_16_64 3
		.amdhsa_dx10_clamp 1
		.amdhsa_ieee_mode 1
		.amdhsa_fp16_overflow 0
		.amdhsa_tg_split 0
		.amdhsa_exception_fp_ieee_invalid_op 0
		.amdhsa_exception_fp_denorm_src 0
		.amdhsa_exception_fp_ieee_div_zero 0
		.amdhsa_exception_fp_ieee_overflow 0
		.amdhsa_exception_fp_ieee_underflow 0
		.amdhsa_exception_fp_ieee_inexact 0
		.amdhsa_exception_int_div_zero 0
	.end_amdhsa_kernel

amdhsa.kernels:
  - .agpr_count:     0
    .args:
      - .actual_access:  read_only
        .address_space:  global
        .offset:         0
        .size:           8
        .value_kind:     global_buffer
      - .actual_access:  read_only
        .address_space:  global
        .offset:         8
        .size:           8
        .value_kind:     global_buffer
      - .actual_access:  write_only
        .address_space:  global
        .offset:         16
        .size:           8
        .value_kind:     global_buffer
      - .actual_access:  write_only
        .address_space:  global
        .offset:         24
        .size:           8
        .value_kind:     global_buffer
    .group_segment_fixed_size: 32320
    .kernarg_segment_align: 8
    .kernarg_segment_size: 32
    .language:       OpenCL C
    .language_version:
      - 2
      - 0
    .max_flat_workgroup_size: 1024
    .name:           _Z6k_finePKjPKtPiPt
    .private_segment_fixed_size: 0
    .sgpr_count:     71
    .sgpr_spill_count: 0
    .symbol:         _Z6k_finePKjPKtPiPt.kd
    .uniform_work_group_size: 1
    .uses_dynamic_stack: false
    .vgpr_count:     54
    .vgpr_spill_count: 0
    .wavefront_size: 64
  - .agpr_count:     0
    .args:
      - .actual_access:  read_only
        .address_space:  global
        .offset:         0
        .size:           8
        .value_kind:     global_buffer
      - .actual_access:  read_only
        .address_space:  global
        .offset:         8
        .size:           8
        .value_kind:     global_buffer
      - .actual_access:  write_only
        .address_space:  global
        .offset:         16
        .size:           8
        .value_kind:     global_buffer
      - .actual_access:  write_only
        .address_space:  global
        .offset:         24
        .size:           8
        .value_kind:     global_buffer
      - .actual_access:  read_only
        .address_space:  global
        .offset:         32
        .size:           8
        .value_kind:     global_buffer
      - .actual_access:  read_only
        .address_space:  global
        .offset:         40
        .size:           8
        .value_kind:     global_buffer
      - .actual_access:  write_only
        .address_space:  global
        .offset:         48
        .size:           8
        .value_kind:     global_buffer
      - .actual_access:  write_only
        .address_space:  global
        .offset:         56
        .size:           8
        .value_kind:     global_buffer
      - .actual_access:  read_only
        .address_space:  global
        .offset:         64
        .size:           8
        .value_kind:     global_buffer
      - .actual_access:  read_only
        .address_space:  global
        .offset:         72
        .size:           8
        .value_kind:     global_buffer
      - .actual_access:  read_only
        .address_space:  global
        .offset:         80
        .size:           8
        .value_kind:     global_buffer
      - .actual_access:  write_only
        .address_space:  global
        .offset:         88
        .size:           8
        .value_kind:     global_buffer
      - .actual_access:  write_only
        .address_space:  global
        .offset:         96
        .size:           8
        .value_kind:     global_buffer
      - .actual_access:  write_only
        .address_space:  global
        .offset:         104
        .size:           8
        .value_kind:     global_buffer
    .group_segment_fixed_size: 53248
    .kernarg_segment_align: 8
    .kernarg_segment_size: 112
    .language:       OpenCL C
    .language_version:
      - 2
      - 0
    .max_flat_workgroup_size: 256
    .name:           _Z8k_stageAPKiS0_PjPtPKfS4_PDF16_S5_S4_S4_S4_S5_PfS6_
    .private_segment_fixed_size: 0
    .sgpr_count:     75
    .sgpr_spill_count: 0
    .symbol:         _Z8k_stageAPKiS0_PjPtPKfS4_PDF16_S5_S4_S4_S4_S5_PfS6_.kd
    .uniform_work_group_size: 1
    .uses_dynamic_stack: false
    .vgpr_count:     158
    .vgpr_spill_count: 0
    .wavefront_size: 64
  - .agpr_count:     4
    .args:
      - .actual_access:  read_only
        .address_space:  global
        .offset:         0
        .size:           8
        .value_kind:     global_buffer
      - .actual_access:  read_only
        .address_space:  global
        .offset:         8
        .size:           8
        .value_kind:     global_buffer
      - .actual_access:  read_only
        .address_space:  global
        .offset:         16
        .size:           8
        .value_kind:     global_buffer
      - .actual_access:  read_only
        .address_space:  global
        .offset:         24
        .size:           8
        .value_kind:     global_buffer
      - .actual_access:  write_only
        .address_space:  global
        .offset:         32
        .size:           8
        .value_kind:     global_buffer
      - .actual_access:  write_only
        .address_space:  global
        .offset:         40
        .size:           8
        .value_kind:     global_buffer
      - .actual_access:  write_only
        .address_space:  global
        .offset:         48
        .size:           8
        .value_kind:     global_buffer
    .group_segment_fixed_size: 19584
    .kernarg_segment_align: 8
    .kernarg_segment_size: 56
    .language:       OpenCL C
    .language_version:
      - 2
      - 0
    .max_flat_workgroup_size: 256
    .name:           _Z7k_gemm2PKDF16_S0_PKfS2_PDF16_PfS4_
    .private_segment_fixed_size: 0
    .sgpr_count:     30
    .sgpr_spill_count: 0
    .symbol:         _Z7k_gemm2PKDF16_S0_PKfS2_PDF16_PfS4_.kd
    .uniform_work_group_size: 1
    .uses_dynamic_stack: false
    .vgpr_count:     84
    .vgpr_spill_count: 0
    .wavefront_size: 64
  - .agpr_count:     12
    .args:
      - .actual_access:  read_only
        .address_space:  global
        .offset:         0
        .size:           8
        .value_kind:     global_buffer
      - .actual_access:  read_only
        .address_space:  global
        .offset:         8
        .size:           8
        .value_kind:     global_buffer
      - .actual_access:  read_only
        .address_space:  global
        .offset:         16
        .size:           8
        .value_kind:     global_buffer
      - .actual_access:  read_only
        .address_space:  global
        .offset:         24
        .size:           8
        .value_kind:     global_buffer
      - .actual_access:  read_only
        .address_space:  global
        .offset:         32
        .size:           8
        .value_kind:     global_buffer
      - .actual_access:  read_only
        .address_space:  global
        .offset:         40
        .size:           8
        .value_kind:     global_buffer
      - .actual_access:  read_only
        .address_space:  global
        .offset:         48
        .size:           8
        .value_kind:     global_buffer
      - .actual_access:  read_only
        .address_space:  global
        .offset:         56
        .size:           8
        .value_kind:     global_buffer
      - .actual_access:  read_only
        .address_space:  global
        .offset:         64
        .size:           8
        .value_kind:     global_buffer
      - .actual_access:  read_only
        .address_space:  global
        .offset:         72
        .size:           8
        .value_kind:     global_buffer
      - .actual_access:  write_only
        .address_space:  global
        .offset:         80
        .size:           8
        .value_kind:     global_buffer
      - .actual_access:  write_only
        .address_space:  global
        .offset:         88
        .size:           8
        .value_kind:     global_buffer
      - .actual_access:  write_only
        .address_space:  global
        .offset:         96
        .size:           8
        .value_kind:     global_buffer
      - .offset:         104
        .size:           4
        .value_kind:     hidden_block_count_x
      - .offset:         108
        .size:           4
        .value_kind:     hidden_block_count_y
      - .offset:         112
        .size:           4
        .value_kind:     hidden_block_count_z
      - .offset:         116
        .size:           2
        .value_kind:     hidden_group_size_x
      - .offset:         118
        .size:           2
        .value_kind:     hidden_group_size_y
      - .offset:         120
        .size:           2
        .value_kind:     hidden_group_size_z
      - .offset:         122
        .size:           2
        .value_kind:     hidden_remainder_x
      - .offset:         124
        .size:           2
        .value_kind:     hidden_remainder_y
      - .offset:         126
        .size:           2
        .value_kind:     hidden_remainder_z
      - .offset:         144
        .size:           8
        .value_kind:     hidden_global_offset_x
      - .offset:         152
        .size:           8
        .value_kind:     hidden_global_offset_y
      - .offset:         160
        .size:           8
        .value_kind:     hidden_global_offset_z
      - .offset:         168
        .size:           2
        .value_kind:     hidden_grid_dims
    .group_segment_fixed_size: 39168
    .kernarg_segment_align: 8
    .kernarg_segment_size: 360
    .language:       OpenCL C
    .language_version:
      - 2
      - 0
    .max_flat_workgroup_size: 256
    .name:           _Z5k_aggILi4ELi128ELi16ELi16ELb0EEvPKiPKtPKDF16_PKfS7_S7_PvS5_S7_S7_PDF16_PfSA_
    .private_segment_fixed_size: 0
    .sgpr_count:     55
    .sgpr_spill_count: 0
    .symbol:         _Z5k_aggILi4ELi128ELi16ELi16ELb0EEvPKiPKtPKDF16_PKfS7_S7_PvS5_S7_S7_PDF16_PfSA_.kd
    .uniform_work_group_size: 1
    .uses_dynamic_stack: false
    .vgpr_count:     124
    .vgpr_spill_count: 0
    .wavefront_size: 64
  - .agpr_count:     0
    .args:
      - .actual_access:  read_only
        .address_space:  global
        .offset:         0
        .size:           8
        .value_kind:     global_buffer
      - .actual_access:  read_only
        .address_space:  global
        .offset:         8
        .size:           8
        .value_kind:     global_buffer
      - .actual_access:  read_only
        .address_space:  global
        .offset:         16
        .size:           8
        .value_kind:     global_buffer
      - .actual_access:  read_only
        .address_space:  global
        .offset:         24
        .size:           8
        .value_kind:     global_buffer
      - .actual_access:  read_only
        .address_space:  global
        .offset:         32
        .size:           8
        .value_kind:     global_buffer
      - .actual_access:  read_only
        .address_space:  global
        .offset:         40
        .size:           8
        .value_kind:     global_buffer
      - .actual_access:  write_only
        .address_space:  global
        .offset:         48
        .size:           8
        .value_kind:     global_buffer
      - .actual_access:  read_only
        .address_space:  global
        .offset:         56
        .size:           8
        .value_kind:     global_buffer
      - .actual_access:  read_only
        .address_space:  global
        .offset:         64
        .size:           8
        .value_kind:     global_buffer
      - .actual_access:  read_only
        .address_space:  global
        .offset:         72
        .size:           8
        .value_kind:     global_buffer
      - .actual_access:  read_only
        .address_space:  global
        .offset:         80
        .size:           8
        .value_kind:     global_buffer
      - .actual_access:  read_only
        .address_space:  global
        .offset:         88
        .size:           8
        .value_kind:     global_buffer
      - .actual_access:  read_only
        .address_space:  global
        .offset:         96
        .size:           8
        .value_kind:     global_buffer
      - .offset:         104
        .size:           4
        .value_kind:     hidden_block_count_x
      - .offset:         108
        .size:           4
        .value_kind:     hidden_block_count_y
      - .offset:         112
        .size:           4
        .value_kind:     hidden_block_count_z
      - .offset:         116
        .size:           2
        .value_kind:     hidden_group_size_x
      - .offset:         118
        .size:           2
        .value_kind:     hidden_group_size_y
      - .offset:         120
        .size:           2
        .value_kind:     hidden_group_size_z
      - .offset:         122
        .size:           2
        .value_kind:     hidden_remainder_x
      - .offset:         124
        .size:           2
        .value_kind:     hidden_remainder_y
      - .offset:         126
        .size:           2
        .value_kind:     hidden_remainder_z
      - .offset:         144
        .size:           8
        .value_kind:     hidden_global_offset_x
      - .offset:         152
        .size:           8
        .value_kind:     hidden_global_offset_y
      - .offset:         160
        .size:           8
        .value_kind:     hidden_global_offset_z
      - .offset:         168
        .size:           2
        .value_kind:     hidden_grid_dims
    .group_segment_fixed_size: 8704
    .kernarg_segment_align: 8
    .kernarg_segment_size: 360
    .language:       OpenCL C
    .language_version:
      - 2
      - 0
    .max_flat_workgroup_size: 256
    .name:           _Z5k_aggILi1ELi40ELi5ELi5ELb1EEvPKiPKtPKDF16_PKfS7_S7_PvS5_S7_S7_PDF16_PfSA_
    .private_segment_fixed_size: 0
    .sgpr_count:     31
    .sgpr_spill_count: 0
    .symbol:         _Z5k_aggILi1ELi40ELi5ELi5ELb1EEvPKiPKtPKDF16_PKfS7_S7_PvS5_S7_S7_PDF16_PfSA_.kd
    .uniform_work_group_size: 1
    .uses_dynamic_stack: false
    .vgpr_count:     76
    .vgpr_spill_count: 0
    .wavefront_size: 64
